# baseline (speedup 1.0000x reference)
.LBB1_14:
	s_or_b64 exec, exec, s[4:5]
	ds_read_b64_tr_b16 v[144:145], v140
	ds_read_b64_tr_b16 v[146:147], v140 offset:1024
	ds_read_b64_tr_b16 v[148:149], v140 offset:2048
	ds_read_b64_tr_b16 v[150:151], v140 offset:3072
	ds_read_b64_tr_b16 v[152:153], v140 offset:4096
	ds_read_b64_tr_b16 v[154:155], v140 offset:5120
	ds_read_b64_tr_b16 v[156:157], v140 offset:6144
	ds_read_b64_tr_b16 v[158:159], v140 offset:7168
	s_or_b32 s12, s12, s16
	v_or_b32_e32 v22, v130, v137
	v_mov_b32_e32 v23, 0
	v_lshl_add_u64 v[2:3], s[12:13], 0, v[22:23]
	v_lshlrev_b64 v[2:3], 6, v[2:3]
	v_lshl_add_u64 v[2:3], s[10:11], 0, v[2:3]
	v_and_b32_e32 v4, 32, v0
	v_mov_b32_e32 v5, v23
	v_lshl_add_u64 v[32:33], v[2:3], 0, v[4:5]
	s_mov_b64 s[0:1], 0x800000
	v_lshl_add_u64 v[16:17], v[32:33], 0, s[0:1]
	s_lshl_b64 s[0:1], s[6:7], 12
	v_mov_b32_e32 v0, s3
	v_or3_b32 v2, s0, v0, v137
	v_rcp_f32_e32 v0, v1
	v_or3_b32 v3, s1, 0, 0
	v_lshlrev_b64 v[2:3], 8, v[2:3]
	v_lshl_add_u64 v[2:3], s[10:11], 0, v[2:3]
	v_mul_f32_e32 v0, 0x42fe0000, v0
	v_mul_f32_e32 v10, 0x3f7fffff, v0
	v_lshl_add_u64 v[2:3], v[2:3], 0, v[130:131]
	v_mov_b32_e32 v137, v23
	v_fmaak_f32 v0, v51, v10, 0x4b400000
	v_fmaak_f32 v1, v50, v10, 0x4b400000
	s_mov_b32 s0, 0xc0c0400
	v_lshl_add_u64 v[6:7], v[2:3], 0, v[136:137]
	v_perm_b32 v0, v0, v1, s0
	v_fmaak_f32 v1, v53, v10, 0x4b400000
	v_fmaak_f32 v2, v52, v10, 0x4b400000
	s_mov_b32 s1, 0x4000c0c
	v_perm_b32 v1, v1, v2, s1
	v_or_b32_e32 v0, v0, v1
	v_fmaak_f32 v1, v55, v10, 0x4b400000
	v_fmaak_f32 v2, v54, v10, 0x4b400000
	v_perm_b32 v1, v1, v2, s0
	v_fmaak_f32 v2, v57, v10, 0x4b400000
	v_fmaak_f32 v3, v56, v10, 0x4b400000
	v_perm_b32 v2, v2, v3, s1
	v_or_b32_e32 v1, v1, v2
	v_fmaak_f32 v2, v59, v10, 0x4b400000
	v_fmaak_f32 v3, v58, v10, 0x4b400000
	v_perm_b32 v2, v2, v3, s0
	v_fmaak_f32 v3, v61, v10, 0x4b400000
	v_fmaak_f32 v8, v60, v10, 0x4b400000
	v_perm_b32 v3, v3, v8, s1
	v_or_b32_e32 v2, v2, v3
	v_fmaak_f32 v3, v63, v10, 0x4b400000
	v_fmaak_f32 v8, v62, v10, 0x4b400000
	v_perm_b32 v3, v3, v8, s0
	v_fmaak_f32 v8, v65, v10, 0x4b400000
	v_fmaak_f32 v9, v64, v10, 0x4b400000
	v_perm_b32 v8, v8, v9, s1
	s_mov_b32 s2, 0x400000
	v_or_b32_e32 v3, v3, v8
	v_add_co_u32_e32 v8, vcc, s2, v6
	v_mov_b32_e32 v11, 0x4b400000
	s_nop 0
	v_addc_co_u32_e32 v9, vcc, 0, v7, vcc
	global_store_dwordx4 v[8:9], v[0:3], off
	v_fmaak_f32 v8, v44, v10, 0x4b400000
	v_fmac_f32_e32 v11, v48, v10
	v_fmaak_f32 v0, v35, v10, 0x4b400000
	v_fmaak_f32 v1, v34, v10, 0x4b400000
	v_perm_b32 v0, v0, v1, s0
	v_fmaak_f32 v1, v37, v10, 0x4b400000
	v_fmaak_f32 v2, v36, v10, 0x4b400000
	v_perm_b32 v1, v1, v2, s1
	v_or_b32_e32 v0, v0, v1
	v_fmaak_f32 v1, v39, v10, 0x4b400000
	v_fmaak_f32 v2, v38, v10, 0x4b400000
	v_perm_b32 v1, v1, v2, s0
	v_fmaak_f32 v2, v41, v10, 0x4b400000
	v_fmaak_f32 v3, v40, v10, 0x4b400000
	v_perm_b32 v2, v2, v3, s1
	v_or_b32_e32 v1, v1, v2
	v_fmaak_f32 v2, v43, v10, 0x4b400000
	v_fmaak_f32 v3, v42, v10, 0x4b400000
	v_perm_b32 v2, v2, v3, s0
	v_fmaak_f32 v3, v45, v10, 0x4b400000
	v_perm_b32 v3, v3, v8, s1
	v_or_b32_e32 v2, v2, v3
	v_fmaak_f32 v3, v47, v10, 0x4b400000
	v_fmaak_f32 v8, v46, v10, 0x4b400000
	v_perm_b32 v3, v3, v8, s0
	v_fmaak_f32 v8, v49, v10, 0x4b400000
	s_mov_b32 s0, 0x402000
	v_perm_b32 v8, v8, v11, s1
	v_add_co_u32_e32 v6, vcc, s0, v6
	v_or_b32_e32 v3, v3, v8
	s_nop 0
	v_addc_co_u32_e32 v7, vcc, 0, v7, vcc
	v_lshl_add_u64 v[4:5], v[22:23], 2, s[8:9]
	global_store_dwordx4 v[6:7], v[0:3], off
	global_load_dword v34, v[4:5], off offset:2048
	s_mov_b32 s0, 0x800000
	s_waitcnt vmcnt(18) lgkmcnt(6)
	v_mfma_f32_32x32x16_bf16 v[0:15], v[144:147], v[118:121], 0
	ds_read_b64_tr_b16 v[144:145], v140 offset:8192
	ds_read_b64_tr_b16 v[146:147], v140 offset:9216
	s_waitcnt lgkmcnt(6)
	v_mfma_f32_32x32x16_bf16 v[0:15], v[148:151], v[114:117], v[0:15]
	ds_read_b64_tr_b16 v[148:149], v140 offset:10240
	ds_read_b64_tr_b16 v[150:151], v140 offset:11264
	s_waitcnt lgkmcnt(6)
	v_mfma_f32_32x32x16_bf16 v[0:15], v[152:155], v[110:113], v[0:15]
	ds_read_b64_tr_b16 v[152:153], v140 offset:12288
	ds_read_b64_tr_b16 v[154:155], v140 offset:13312
	s_waitcnt vmcnt(11) lgkmcnt(6)
	v_mfma_f32_32x32x16_bf16 v[0:15], v[156:159], v[122:125], v[0:15]
	ds_read_b64_tr_b16 v[156:157], v140 offset:14336
	ds_read_b64_tr_b16 v[158:159], v140 offset:15360
	s_waitcnt lgkmcnt(6)
	v_mfma_f32_32x32x16_bf16 v[0:15], v[144:147], v[102:105], v[0:15]
	ds_read_b64_tr_b16 v[144:145], v140 offset:16384
	ds_read_b64_tr_b16 v[146:147], v140 offset:17408
	s_waitcnt lgkmcnt(6)
	v_mfma_f32_32x32x16_bf16 v[0:15], v[148:151], v[94:97], v[0:15]
	ds_read_b64_tr_b16 v[148:149], v140 offset:18432
	ds_read_b64_tr_b16 v[150:151], v140 offset:19456
	s_waitcnt lgkmcnt(6)
	v_mfma_f32_32x32x16_bf16 v[0:15], v[152:155], v[82:85], v[0:15]
	ds_read_b64_tr_b16 v[152:153], v140 offset:20480
	ds_read_b64_tr_b16 v[154:155], v140 offset:21504
	s_waitcnt lgkmcnt(6)
	v_mfma_f32_32x32x16_bf16 v[0:15], v[156:159], v[90:93], v[0:15]
	ds_read_b64_tr_b16 v[156:157], v140 offset:22528
	ds_read_b64_tr_b16 v[158:159], v140 offset:23552
	s_waitcnt lgkmcnt(6)
	v_mfma_f32_32x32x16_bf16 v[0:15], v[144:147], v[106:109], v[0:15]
	ds_read_b64_tr_b16 v[144:145], v140 offset:24576
	ds_read_b64_tr_b16 v[146:147], v140 offset:25600
	s_waitcnt vmcnt(10) lgkmcnt(6)
	v_mfma_f32_32x32x16_bf16 v[0:15], v[148:151], v[98:101], v[0:15]
	ds_read_b64_tr_b16 v[148:149], v140 offset:26624
	ds_read_b64_tr_b16 v[150:151], v140 offset:27648
	s_waitcnt vmcnt(9) lgkmcnt(6)
	v_mfma_f32_32x32x16_bf16 v[0:15], v[152:155], v[86:89], v[0:15]
	ds_read_b64_tr_b16 v[152:153], v140 offset:28672
	ds_read_b64_tr_b16 v[154:155], v140 offset:29696
	s_waitcnt vmcnt(8) lgkmcnt(6)
	v_mfma_f32_32x32x16_bf16 v[0:15], v[156:159], v[70:73], v[0:15]
	ds_read_b64_tr_b16 v[156:157], v140 offset:30720
	ds_read_b64_tr_b16 v[158:159], v140 offset:31744
	s_waitcnt vmcnt(7) lgkmcnt(6)
	v_mfma_f32_32x32x16_bf16 v[0:15], v[144:147], v[28:31], v[0:15]
	ds_read_b64_tr_b16 v[144:145], v140 offset:512
	ds_read_b64_tr_b16 v[146:147], v140 offset:1536
	s_waitcnt vmcnt(6) lgkmcnt(6)
	v_mfma_f32_32x32x16_bf16 v[0:15], v[148:151], v[66:69], v[0:15]
	ds_read_b64_tr_b16 v[148:149], v140 offset:2560
	ds_read_b64_tr_b16 v[150:151], v140 offset:3584
	s_waitcnt vmcnt(5) lgkmcnt(6)
	v_mfma_f32_32x32x16_bf16 v[0:15], v[152:155], v[24:27], v[0:15]
	ds_read_b64_tr_b16 v[152:153], v140 offset:4608
	ds_read_b64_tr_b16 v[154:155], v140 offset:5632
	s_waitcnt vmcnt(4) lgkmcnt(6)
	v_mfma_f32_32x32x16_bf16 v[0:15], v[156:159], v[18:21], v[0:15]
	ds_read_b64_tr_b16 v[156:157], v140 offset:6656
	ds_read_b64_tr_b16 v[158:159], v140 offset:7680
	s_waitcnt vmcnt(0)
	s_nop 10
	v_add_f32_e32 v22, v34, v0
	v_add_f32_e32 v1, v34, v1
	v_mov_b32_e32 v0, v23
	v_cvt_pk_fp8_f32 v0, v22, v1
	v_add_f32_e32 v1, v34, v2
	v_add_f32_e32 v2, v34, v3
	v_add_f32_e32 v3, v34, v5
	v_cvt_pk_fp8_f32 v0, v1, v2 op_sel:[0,0,1]
	v_add_f32_e32 v2, v34, v4
	v_mov_b32_e32 v1, v23
	v_cvt_pk_fp8_f32 v1, v2, v3
	v_add_f32_e32 v2, v34, v6
	v_add_f32_e32 v3, v34, v7
	v_add_f32_e32 v4, v34, v9
	v_cvt_pk_fp8_f32 v1, v2, v3 op_sel:[0,0,1]
	v_add_f32_e32 v3, v34, v8
	v_mov_b32_e32 v2, v23
	v_cvt_pk_fp8_f32 v2, v3, v4
	v_add_f32_e32 v3, v34, v10
	v_add_f32_e32 v4, v34, v11
	v_add_f32_e32 v5, v34, v13
	v_cvt_pk_fp8_f32 v2, v3, v4 op_sel:[0,0,1]
	v_add_f32_e32 v4, v34, v12
	v_mov_b32_e32 v3, v23
	v_cvt_pk_fp8_f32 v3, v4, v5
	v_add_f32_e32 v4, v34, v14
	v_add_f32_e32 v5, v34, v15
	v_mov_b32_e32 v22, v23
	v_cvt_pk_fp8_f32 v3, v4, v5 op_sel:[0,0,1]
	v_add_co_u32_e32 v4, vcc, s0, v32
	s_nop 1
	v_addc_co_u32_e32 v5, vcc, 0, v33, vcc
	global_store_dwordx4 v[4:5], v[0:3], off
	s_nop 1
	s_waitcnt lgkmcnt(6)
	v_mfma_f32_32x32x16_bf16 v[0:15], v[144:147], v[118:121], 0
	ds_read_b64_tr_b16 v[144:145], v140 offset:8704
	ds_read_b64_tr_b16 v[146:147], v140 offset:9728
	s_waitcnt lgkmcnt(6)
	v_mfma_f32_32x32x16_bf16 v[0:15], v[148:151], v[114:117], v[0:15]
	ds_read_b64_tr_b16 v[148:149], v140 offset:10752
	ds_read_b64_tr_b16 v[150:151], v140 offset:11776
	s_waitcnt lgkmcnt(6)
	v_mfma_f32_32x32x16_bf16 v[0:15], v[152:155], v[110:113], v[0:15]
	ds_read_b64_tr_b16 v[152:153], v140 offset:12800
	ds_read_b64_tr_b16 v[154:155], v140 offset:13824
	s_waitcnt lgkmcnt(6)
	v_mfma_f32_32x32x16_bf16 v[0:15], v[156:159], v[122:125], v[0:15]
	ds_read_b64_tr_b16 v[156:157], v140 offset:14848
	ds_read_b64_tr_b16 v[158:159], v140 offset:15872
	s_waitcnt lgkmcnt(6)
	v_mfma_f32_32x32x16_bf16 v[0:15], v[144:147], v[102:105], v[0:15]
	ds_read_b64_tr_b16 v[144:145], v140 offset:16896
	ds_read_b64_tr_b16 v[146:147], v140 offset:17920
	s_waitcnt lgkmcnt(6)
	v_mfma_f32_32x32x16_bf16 v[0:15], v[148:151], v[94:97], v[0:15]
	ds_read_b64_tr_b16 v[148:149], v140 offset:18944
	ds_read_b64_tr_b16 v[150:151], v140 offset:19968
	s_waitcnt lgkmcnt(6)
	v_mfma_f32_32x32x16_bf16 v[0:15], v[152:155], v[82:85], v[0:15]
	ds_read_b64_tr_b16 v[152:153], v140 offset:20992
	ds_read_b64_tr_b16 v[154:155], v140 offset:22016
	s_waitcnt lgkmcnt(6)
	v_mfma_f32_32x32x16_bf16 v[0:15], v[156:159], v[90:93], v[0:15]
	ds_read_b64_tr_b16 v[156:157], v140 offset:23040
	ds_read_b64_tr_b16 v[158:159], v140 offset:24064
	s_waitcnt lgkmcnt(6)
	v_mfma_f32_32x32x16_bf16 v[0:15], v[144:147], v[106:109], v[0:15]
	ds_read_b64_tr_b16 v[144:145], v140 offset:25088
	ds_read_b64_tr_b16 v[146:147], v140 offset:26112
	s_waitcnt lgkmcnt(6)
	v_mfma_f32_32x32x16_bf16 v[0:15], v[148:151], v[98:101], v[0:15]
	ds_read_b64_tr_b16 v[148:149], v140 offset:27136
	ds_read_b64_tr_b16 v[150:151], v140 offset:28160
	s_waitcnt lgkmcnt(6)
	v_mfma_f32_32x32x16_bf16 v[0:15], v[152:155], v[86:89], v[0:15]
	ds_read_b64_tr_b16 v[152:153], v140 offset:29184
	ds_read_b64_tr_b16 v[154:155], v140 offset:30208
	s_waitcnt lgkmcnt(6)
	v_mfma_f32_32x32x16_bf16 v[0:15], v[156:159], v[70:73], v[0:15]
	ds_read_b64_tr_b16 v[156:157], v140 offset:31232
	ds_read_b64_tr_b16 v[158:159], v140 offset:32256
	s_waitcnt lgkmcnt(6)
	v_mfma_f32_32x32x16_bf16 v[0:15], v[144:147], v[28:31], v[0:15]
	s_waitcnt lgkmcnt(4)
	v_mfma_f32_32x32x16_bf16 v[0:15], v[148:151], v[66:69], v[0:15]
	s_waitcnt lgkmcnt(2)
	v_mfma_f32_32x32x16_bf16 v[0:15], v[152:155], v[24:27], v[0:15]
	s_waitcnt lgkmcnt(0)
	v_mfma_f32_32x32x16_bf16 v[0:15], v[156:159], v[18:21], v[0:15]
	v_mov_b32_e32 v20, v23
	v_mov_b32_e32 v21, v23
	s_nop 9
	v_add_f32_e32 v0, v34, v0
	v_add_f32_e32 v1, v34, v1
	v_cvt_pk_fp8_f32 v20, v0, v1
	v_add_f32_e32 v0, v34, v2
	v_add_f32_e32 v1, v34, v3
	v_cvt_pk_fp8_f32 v20, v0, v1 op_sel:[0,0,1]
	v_add_f32_e32 v0, v34, v4
	v_add_f32_e32 v1, v34, v5
	v_cvt_pk_fp8_f32 v21, v0, v1
	v_add_f32_e32 v0, v34, v6
	v_add_f32_e32 v1, v34, v7
	v_cvt_pk_fp8_f32 v21, v0, v1 op_sel:[0,0,1]
	v_add_f32_e32 v0, v34, v8
	v_add_f32_e32 v1, v34, v9
	v_cvt_pk_fp8_f32 v22, v0, v1
	v_add_f32_e32 v0, v34, v10
	v_add_f32_e32 v1, v34, v11
	v_cvt_pk_fp8_f32 v22, v0, v1 op_sel:[0,0,1]
	v_add_f32_e32 v0, v34, v12
	v_add_f32_e32 v1, v34, v13
	v_cvt_pk_fp8_f32 v23, v0, v1
	v_add_f32_e32 v0, v34, v14
	v_add_f32_e32 v1, v34, v15
	v_cvt_pk_fp8_f32 v23, v0, v1 op_sel:[0,0,1]
	global_store_dwordx4 v[16:17], v[20:23], off offset:16
	s_endpgm
